# baseline (speedup 1.0000x reference)
.Lep1_prej:
	s_waitcnt lgkmcnt(7)
	s_barrier
	s_cmp_eq_u64 s[6:7], 0
	s_cbranch_scc0 .Lep1_k1
	s_mul_i32 s43, s36, 0x5000
	s_add_i32 s43, s43, s86
	s_add_u32 s40, s18, s43
	s_addc_u32 s41, s19, 0
	ds_read2st64_b32 v[50:51], v221 offset0:0 offset1:1
	ds_read2st64_b32 v[52:53], v221 offset0:2 offset1:3
	ds_read2st64_b32 v[54:55], v221 offset0:4 offset1:5
	ds_read2st64_b32 v[56:57], v221 offset0:6 offset1:7
	ds_read2st64_b32 v[58:59], v221 offset0:8 offset1:9
	ds_read2st64_b32 v[60:61], v221 offset0:10 offset1:11
	s_waitcnt lgkmcnt(12)
	v_fma_f32 v78, -v76, v77, 0
	s_waitcnt lgkmcnt(4)
	v_pk_add_f32 v[34:35], v[34:35], v[50:51]
	v_pk_add_f32 v[36:37], v[36:37], v[52:53]
	v_pk_add_f32 v[34:35], v[34:35], v[78:79] op_sel_hi:[1,0]
	v_pk_add_f32 v[36:37], v[36:37], v[78:79] op_sel_hi:[1,0]
	v_pk_fma_f32 v[34:35], v[62:63], v[76:77], v[34:35] op_sel:[0,1,0] op_sel_hi:[1,1,1]
	v_pk_fma_f32 v[36:37], v[64:65], v[76:77], v[36:37] op_sel:[0,1,0] op_sel_hi:[1,1,1]
	v_pk_mul_f32 v[20:21], v[34:35], v[34:35]
	v_pk_add_f32 v[18:19], v[34:35], v[36:37]
	v_pk_fma_f32 v[20:21], v[36:37], v[36:37], v[20:21]
	s_waitcnt lgkmcnt(2)
	v_pk_add_f32 v[38:39], v[38:39], v[54:55]
	v_pk_add_f32 v[40:41], v[40:41], v[56:57]
	v_pk_add_f32 v[38:39], v[38:39], v[78:79] op_sel_hi:[1,0]
	v_pk_add_f32 v[40:41], v[40:41], v[78:79] op_sel_hi:[1,0]
	v_pk_fma_f32 v[38:39], v[68:69], v[76:77], v[38:39] op_sel:[0,1,0] op_sel_hi:[1,1,1]
	v_pk_fma_f32 v[40:41], v[70:71], v[76:77], v[40:41] op_sel:[0,1,0] op_sel_hi:[1,1,1]
	v_pk_add_f32 v[18:19], v[18:19], v[38:39]
	v_pk_fma_f32 v[20:21], v[38:39], v[38:39], v[20:21]
	v_pk_add_f32 v[18:19], v[18:19], v[40:41]
	v_pk_fma_f32 v[20:21], v[40:41], v[40:41], v[20:21]
	s_waitcnt lgkmcnt(0)
	v_pk_add_f32 v[42:43], v[42:43], v[58:59]
	v_pk_add_f32 v[44:45], v[44:45], v[60:61]
	v_pk_add_f32 v[42:43], v[42:43], v[78:79] op_sel_hi:[1,0]
	v_pk_add_f32 v[44:45], v[44:45], v[78:79] op_sel_hi:[1,0]
	v_pk_fma_f32 v[42:43], v[72:73], v[76:77], v[42:43] op_sel:[0,1,0] op_sel_hi:[1,1,1]
	v_pk_fma_f32 v[44:45], v[74:75], v[76:77], v[44:45] op_sel:[0,1,0] op_sel_hi:[1,1,1]
	v_pk_add_f32 v[18:19], v[18:19], v[42:43]
	v_pk_fma_f32 v[20:21], v[42:43], v[42:43], v[20:21]
	v_pk_add_f32 v[18:19], v[18:19], v[44:45]
	v_pk_fma_f32 v[20:21], v[44:45], v[44:45], v[20:21]
	ds_read2st64_b32 v[50:51], v221 offset0:12 offset1:13
	ds_read2st64_b32 v[52:53], v221 offset0:14 offset1:15
	ds_read2st64_b32 v[54:55], v221 offset0:16 offset1:17
	ds_read2st64_b32 v[56:57], v221 offset0:18 offset1:19
	ds_read2st64_b32 v[58:59], v221 offset0:20 offset1:21
	ds_read2st64_b32 v[60:61], v221 offset0:22 offset1:23
	ds_read2st64_b32 v[62:63], v67 offset0:48 offset1:50
	ds_read2st64_b32 v[64:65], v67 offset0:52 offset1:54
	ds_read2st64_b32 v[68:69], v67 offset0:64 offset1:66
	ds_read2st64_b32 v[70:71], v67 offset0:68 offset1:70
	ds_read2st64_b32 v[72:73], v67 offset0:80 offset1:82
	ds_read2st64_b32 v[74:75], v67 offset0:84 offset1:86
	s_barrier
	ds_read_b32 v80, v236
	s_waitcnt lgkmcnt(5)
	v_pk_add_f32 v[46:47], v[46:47], v[50:51]
	v_pk_add_f32 v[48:49], v[48:49], v[52:53]
	v_pk_add_f32 v[46:47], v[46:47], v[78:79] op_sel_hi:[1,0]
	v_pk_add_f32 v[48:49], v[48:49], v[78:79] op_sel_hi:[1,0]
	v_pk_fma_f32 v[46:47], v[62:63], v[76:77], v[46:47] op_sel:[0,1,0] op_sel_hi:[1,1,1]
	v_pk_fma_f32 v[48:49], v[64:65], v[76:77], v[48:49] op_sel:[0,1,0] op_sel_hi:[1,1,1]
	v_pk_add_f32 v[18:19], v[18:19], v[46:47]
	v_pk_fma_f32 v[20:21], v[46:47], v[46:47], v[20:21]
	v_pk_add_f32 v[18:19], v[18:19], v[48:49]
	v_pk_fma_f32 v[20:21], v[48:49], v[48:49], v[20:21]
	s_waitcnt lgkmcnt(3)
	v_pk_add_f32 v[2:3], v[2:3], v[54:55]
	v_pk_add_f32 v[4:5], v[4:5], v[56:57]
	v_pk_add_f32 v[2:3], v[2:3], v[78:79] op_sel_hi:[1,0]
	v_pk_add_f32 v[4:5], v[4:5], v[78:79] op_sel_hi:[1,0]
	v_pk_fma_f32 v[2:3], v[68:69], v[76:77], v[2:3] op_sel:[0,1,0] op_sel_hi:[1,1,1]
	v_pk_fma_f32 v[4:5], v[70:71], v[76:77], v[4:5] op_sel:[0,1,0] op_sel_hi:[1,1,1]
	v_pk_add_f32 v[18:19], v[18:19], v[2:3]
	v_pk_fma_f32 v[20:21], v[2:3], v[2:3], v[20:21]
	v_pk_add_f32 v[18:19], v[18:19], v[4:5]
	v_pk_fma_f32 v[20:21], v[4:5], v[4:5], v[20:21]
	s_waitcnt lgkmcnt(1)
	v_pk_add_f32 v[6:7], v[6:7], v[58:59]
	v_pk_add_f32 v[8:9], v[8:9], v[60:61]
	v_pk_add_f32 v[6:7], v[6:7], v[78:79] op_sel_hi:[1,0]
	v_pk_add_f32 v[8:9], v[8:9], v[78:79] op_sel_hi:[1,0]
	v_pk_fma_f32 v[6:7], v[72:73], v[76:77], v[6:7] op_sel:[0,1,0] op_sel_hi:[1,1,1]
	v_pk_fma_f32 v[8:9], v[74:75], v[76:77], v[8:9] op_sel:[0,1,0] op_sel_hi:[1,1,1]
	v_pk_add_f32 v[18:19], v[18:19], v[6:7]
	v_pk_fma_f32 v[20:21], v[6:7], v[6:7], v[20:21]
	v_pk_add_f32 v[18:19], v[18:19], v[8:9]
	v_pk_fma_f32 v[20:21], v[8:9], v[8:9], v[20:21]
	v_add_f32_e32 v18, v18, v19
	v_add_f32_e32 v20, v20, v21
	s_nop 1
	v_permlane32_swap_b32_e32 v18, v20
	v_add_f32_e32 v22, v18, v20
	s_branch .Lep1_wr0
.Lep1_k1:
	s_setprio 2
	ds_read2st64_b32 v[50:51], v221 offset0:24 offset1:25
	ds_read2st64_b32 v[52:53], v221 offset0:26 offset1:27
	ds_read2st64_b32 v[54:55], v221 offset0:28 offset1:29
	ds_read2st64_b32 v[56:57], v221 offset0:30 offset1:31
	ds_read2st64_b32 v[58:59], v221 offset0:32 offset1:33
	ds_read2st64_b32 v[60:61], v221 offset0:34 offset1:35
	s_waitcnt lgkmcnt(12)
	v_fma_f32 v78, -v76, v77, 0
	s_waitcnt lgkmcnt(4)
	v_pk_add_f32 v[10:11], v[10:11], v[50:51]
	v_pk_add_f32 v[12:13], v[12:13], v[52:53]
	v_pk_add_f32 v[10:11], v[10:11], v[78:79] op_sel_hi:[1,0]
	v_pk_add_f32 v[12:13], v[12:13], v[78:79] op_sel_hi:[1,0]
	v_pk_fma_f32 v[10:11], v[62:63], v[76:77], v[10:11] op_sel:[0,1,0] op_sel_hi:[1,1,1]
	v_pk_fma_f32 v[12:13], v[64:65], v[76:77], v[12:13] op_sel:[0,1,0] op_sel_hi:[1,1,1]
	v_pk_mul_f32 v[36:37], v[10:11], v[10:11]
	v_pk_add_f32 v[34:35], v[10:11], v[12:13]
	v_pk_fma_f32 v[36:37], v[12:13], v[12:13], v[36:37]
	s_waitcnt lgkmcnt(2)
	v_pk_add_f32 v[14:15], v[14:15], v[54:55]
	v_pk_add_f32 v[16:17], v[16:17], v[56:57]
	v_pk_add_f32 v[14:15], v[14:15], v[78:79] op_sel_hi:[1,0]
	v_pk_add_f32 v[16:17], v[16:17], v[78:79] op_sel_hi:[1,0]
	v_pk_fma_f32 v[14:15], v[68:69], v[76:77], v[14:15] op_sel:[0,1,0] op_sel_hi:[1,1,1]
	v_pk_fma_f32 v[16:17], v[70:71], v[76:77], v[16:17] op_sel:[0,1,0] op_sel_hi:[1,1,1]
	v_pk_add_f32 v[34:35], v[34:35], v[14:15]
	v_pk_fma_f32 v[36:37], v[14:15], v[14:15], v[36:37]
	v_pk_add_f32 v[34:35], v[34:35], v[16:17]
	v_pk_fma_f32 v[36:37], v[16:17], v[16:17], v[36:37]
	s_waitcnt lgkmcnt(0)
	v_pk_add_f32 v[18:19], v[18:19], v[58:59]
	v_pk_add_f32 v[20:21], v[20:21], v[60:61]
	v_pk_add_f32 v[18:19], v[18:19], v[78:79] op_sel_hi:[1,0]
	v_pk_add_f32 v[20:21], v[20:21], v[78:79] op_sel_hi:[1,0]
	v_pk_fma_f32 v[18:19], v[72:73], v[76:77], v[18:19] op_sel:[0,1,0] op_sel_hi:[1,1,1]
	v_pk_fma_f32 v[20:21], v[74:75], v[76:77], v[20:21] op_sel:[0,1,0] op_sel_hi:[1,1,1]
	v_pk_add_f32 v[34:35], v[34:35], v[18:19]
	v_pk_fma_f32 v[36:37], v[18:19], v[18:19], v[36:37]
	v_pk_add_f32 v[34:35], v[34:35], v[20:21]
	v_pk_fma_f32 v[36:37], v[20:21], v[20:21], v[36:37]
	ds_read2st64_b32 v[50:51], v221 offset0:36 offset1:37
	ds_read2st64_b32 v[52:53], v221 offset0:38 offset1:39
	ds_read2st64_b32 v[62:63], v67 offset0:144 offset1:146
	ds_read2st64_b32 v[64:65], v67 offset0:148 offset1:150
	s_waitcnt lgkmcnt(0)
	v_pk_add_f32 v[22:23], v[22:23], v[50:51]
	v_pk_add_f32 v[24:25], v[24:25], v[52:53]
	v_pk_add_f32 v[22:23], v[22:23], v[78:79] op_sel_hi:[1,0]
	v_pk_add_f32 v[24:25], v[24:25], v[78:79] op_sel_hi:[1,0]
	v_pk_fma_f32 v[22:23], v[62:63], v[76:77], v[22:23] op_sel:[0,1,0] op_sel_hi:[1,1,1]
	v_pk_fma_f32 v[24:25], v[64:65], v[76:77], v[24:25] op_sel:[0,1,0] op_sel_hi:[1,1,1]
	v_pk_add_f32 v[34:35], v[34:35], v[22:23]
	v_pk_fma_f32 v[36:37], v[22:23], v[22:23], v[36:37]
	v_pk_add_f32 v[34:35], v[34:35], v[24:25]
	v_pk_fma_f32 v[36:37], v[24:25], v[24:25], v[36:37]
	s_mov_b64 s[40:41], exec
	s_and_b64 exec, exec, s[0:1]
	ds_read2st64_b32 v[50:51], v221 offset0:40 offset1:41
	ds_read2st64_b32 v[52:53], v221 offset0:42 offset1:43
	ds_read2st64_b32 v[62:63], v67 offset0:160 offset1:162
	ds_read2st64_b32 v[64:65], v67 offset0:164 offset1:166
	s_waitcnt lgkmcnt(0)
	v_pk_add_f32 v[26:27], v[26:27], v[50:51]
	v_pk_add_f32 v[28:29], v[28:29], v[52:53]
	v_pk_add_f32 v[26:27], v[26:27], v[78:79] op_sel_hi:[1,0]
	v_pk_add_f32 v[28:29], v[28:29], v[78:79] op_sel_hi:[1,0]
	v_pk_fma_f32 v[26:27], v[62:63], v[76:77], v[26:27] op_sel:[0,1,0] op_sel_hi:[1,1,1]
	v_pk_fma_f32 v[28:29], v[64:65], v[76:77], v[28:29] op_sel:[0,1,0] op_sel_hi:[1,1,1]
	v_pk_add_f32 v[34:35], v[34:35], v[26:27]
	v_pk_fma_f32 v[36:37], v[26:27], v[26:27], v[36:37]
	v_pk_add_f32 v[34:35], v[34:35], v[28:29]
	v_pk_fma_f32 v[36:37], v[28:29], v[28:29], v[36:37]
	s_mov_b64 exec, s[40:41]
	v_add_f32_e32 v34, v34, v35
	v_add_f32_e32 v36, v36, v37
	s_nop 1
	v_permlane32_swap_b32_e32 v34, v36
	v_add_f32_e32 v38, v34, v36
	ds_write_b32 v236, v38

.Lep2_prej:
	s_waitcnt lgkmcnt(7)
	s_barrier
	s_cmp_eq_u64 s[6:7], 0
	s_cbranch_scc0 .Lep2_k1
	s_mul_i32 s43, s36, 0x5000
	s_addk_i32 s43, 0x2800
	s_add_i32 s43, s43, s86
	s_add_u32 s40, s18, s43
	s_addc_u32 s41, s19, 0
	ds_read2st64_b32 v[50:51], v221 offset0:0 offset1:1
	ds_read2st64_b32 v[52:53], v221 offset0:2 offset1:3
	ds_read2st64_b32 v[54:55], v221 offset0:4 offset1:5
	ds_read2st64_b32 v[56:57], v221 offset0:6 offset1:7
	ds_read2st64_b32 v[58:59], v221 offset0:8 offset1:9
	ds_read2st64_b32 v[60:61], v221 offset0:10 offset1:11
	s_waitcnt lgkmcnt(12)
	v_fma_f32 v78, -v76, v77, v173
	s_waitcnt lgkmcnt(4)
	v_pk_add_f32 v[34:35], v[34:35], v[50:51]
	v_pk_add_f32 v[36:37], v[36:37], v[52:53]
	v_pk_add_f32 v[34:35], v[34:35], v[78:79] op_sel_hi:[1,0]
	v_pk_add_f32 v[36:37], v[36:37], v[78:79] op_sel_hi:[1,0]
	v_pk_fma_f32 v[34:35], v[62:63], v[76:77], v[34:35] op_sel:[0,1,0] op_sel_hi:[1,1,1]
	v_pk_fma_f32 v[36:37], v[64:65], v[76:77], v[36:37] op_sel:[0,1,0] op_sel_hi:[1,1,1]
	v_pk_mul_f32 v[20:21], v[34:35], v[34:35]
	v_pk_add_f32 v[18:19], v[34:35], v[36:37]
	v_pk_fma_f32 v[20:21], v[36:37], v[36:37], v[20:21]
	s_waitcnt lgkmcnt(2)
	v_pk_add_f32 v[38:39], v[38:39], v[54:55]
	v_pk_add_f32 v[40:41], v[40:41], v[56:57]
	v_pk_add_f32 v[38:39], v[38:39], v[78:79] op_sel_hi:[1,0]
	v_pk_add_f32 v[40:41], v[40:41], v[78:79] op_sel_hi:[1,0]
	v_pk_fma_f32 v[38:39], v[68:69], v[76:77], v[38:39] op_sel:[0,1,0] op_sel_hi:[1,1,1]
	v_pk_fma_f32 v[40:41], v[70:71], v[76:77], v[40:41] op_sel:[0,1,0] op_sel_hi:[1,1,1]
	v_pk_add_f32 v[18:19], v[18:19], v[38:39]
	v_pk_fma_f32 v[20:21], v[38:39], v[38:39], v[20:21]
	v_pk_add_f32 v[18:19], v[18:19], v[40:41]
	v_pk_fma_f32 v[20:21], v[40:41], v[40:41], v[20:21]
	s_waitcnt lgkmcnt(0)
	v_pk_add_f32 v[42:43], v[42:43], v[58:59]
	v_pk_add_f32 v[44:45], v[44:45], v[60:61]
	v_pk_add_f32 v[42:43], v[42:43], v[78:79] op_sel_hi:[1,0]
	v_pk_add_f32 v[44:45], v[44:45], v[78:79] op_sel_hi:[1,0]
	v_pk_fma_f32 v[42:43], v[72:73], v[76:77], v[42:43] op_sel:[0,1,0] op_sel_hi:[1,1,1]
	v_pk_fma_f32 v[44:45], v[74:75], v[76:77], v[44:45] op_sel:[0,1,0] op_sel_hi:[1,1,1]
	v_pk_add_f32 v[18:19], v[18:19], v[42:43]
	v_pk_fma_f32 v[20:21], v[42:43], v[42:43], v[20:21]
	v_pk_add_f32 v[18:19], v[18:19], v[44:45]
	v_pk_fma_f32 v[20:21], v[44:45], v[44:45], v[20:21]
	ds_read2st64_b32 v[50:51], v221 offset0:12 offset1:13
	ds_read2st64_b32 v[52:53], v221 offset0:14 offset1:15
	ds_read2st64_b32 v[54:55], v221 offset0:16 offset1:17
	ds_read2st64_b32 v[56:57], v221 offset0:18 offset1:19
	ds_read2st64_b32 v[58:59], v221 offset0:20 offset1:21
	ds_read2st64_b32 v[60:61], v221 offset0:22 offset1:23
	ds_read2st64_b32 v[62:63], v67 offset0:48 offset1:50
	ds_read2st64_b32 v[64:65], v67 offset0:52 offset1:54
	ds_read2st64_b32 v[68:69], v67 offset0:64 offset1:66
	ds_read2st64_b32 v[70:71], v67 offset0:68 offset1:70
	ds_read2st64_b32 v[72:73], v67 offset0:80 offset1:82
	ds_read2st64_b32 v[74:75], v67 offset0:84 offset1:86
	s_barrier
	ds_read_b32 v80, v236
	s_waitcnt lgkmcnt(5)
	v_pk_add_f32 v[46:47], v[46:47], v[50:51]
	v_pk_add_f32 v[48:49], v[48:49], v[52:53]
	v_pk_add_f32 v[46:47], v[46:47], v[78:79] op_sel_hi:[1,0]
	v_pk_add_f32 v[48:49], v[48:49], v[78:79] op_sel_hi:[1,0]
	v_pk_fma_f32 v[46:47], v[62:63], v[76:77], v[46:47] op_sel:[0,1,0] op_sel_hi:[1,1,1]
	v_pk_fma_f32 v[48:49], v[64:65], v[76:77], v[48:49] op_sel:[0,1,0] op_sel_hi:[1,1,1]
	v_pk_add_f32 v[18:19], v[18:19], v[46:47]
	v_pk_fma_f32 v[20:21], v[46:47], v[46:47], v[20:21]
	v_pk_add_f32 v[18:19], v[18:19], v[48:49]
	v_pk_fma_f32 v[20:21], v[48:49], v[48:49], v[20:21]
	s_waitcnt lgkmcnt(3)
	v_pk_add_f32 v[2:3], v[2:3], v[54:55]
	v_pk_add_f32 v[4:5], v[4:5], v[56:57]
	v_pk_add_f32 v[2:3], v[2:3], v[78:79] op_sel_hi:[1,0]
	v_pk_add_f32 v[4:5], v[4:5], v[78:79] op_sel_hi:[1,0]
	v_pk_fma_f32 v[2:3], v[68:69], v[76:77], v[2:3] op_sel:[0,1,0] op_sel_hi:[1,1,1]
	v_pk_fma_f32 v[4:5], v[70:71], v[76:77], v[4:5] op_sel:[0,1,0] op_sel_hi:[1,1,1]
	v_pk_add_f32 v[18:19], v[18:19], v[2:3]
	v_pk_fma_f32 v[20:21], v[2:3], v[2:3], v[20:21]
	v_pk_add_f32 v[18:19], v[18:19], v[4:5]
	v_pk_fma_f32 v[20:21], v[4:5], v[4:5], v[20:21]
	s_waitcnt lgkmcnt(1)
	v_pk_add_f32 v[6:7], v[6:7], v[58:59]
	v_pk_add_f32 v[8:9], v[8:9], v[60:61]
	v_pk_add_f32 v[6:7], v[6:7], v[78:79] op_sel_hi:[1,0]
	v_pk_add_f32 v[8:9], v[8:9], v[78:79] op_sel_hi:[1,0]
	v_pk_fma_f32 v[6:7], v[72:73], v[76:77], v[6:7] op_sel:[0,1,0] op_sel_hi:[1,1,1]
	v_pk_fma_f32 v[8:9], v[74:75], v[76:77], v[8:9] op_sel:[0,1,0] op_sel_hi:[1,1,1]
	v_pk_add_f32 v[18:19], v[18:19], v[6:7]
	v_pk_fma_f32 v[20:21], v[6:7], v[6:7], v[20:21]
	v_pk_add_f32 v[18:19], v[18:19], v[8:9]
	v_pk_fma_f32 v[20:21], v[8:9], v[8:9], v[20:21]
	v_add_f32_e32 v18, v18, v19
	v_add_f32_e32 v20, v20, v21
	s_nop 1
	v_permlane32_swap_b32_e32 v18, v20
	v_add_f32_e32 v22, v18, v20
	s_branch .Lep2_wr0
.Lep2_k1:
	s_setprio 2
	ds_read2st64_b32 v[50:51], v221 offset0:24 offset1:25
	ds_read2st64_b32 v[52:53], v221 offset0:26 offset1:27
	ds_read2st64_b32 v[54:55], v221 offset0:28 offset1:29
	ds_read2st64_b32 v[56:57], v221 offset0:30 offset1:31
	ds_read2st64_b32 v[58:59], v221 offset0:32 offset1:33
	ds_read2st64_b32 v[60:61], v221 offset0:34 offset1:35
	s_waitcnt lgkmcnt(12)
	v_fma_f32 v78, -v76, v77, v173
	s_waitcnt lgkmcnt(4)
	v_pk_add_f32 v[10:11], v[10:11], v[50:51]
	v_pk_add_f32 v[12:13], v[12:13], v[52:53]
	v_pk_add_f32 v[10:11], v[10:11], v[78:79] op_sel_hi:[1,0]
	v_pk_add_f32 v[12:13], v[12:13], v[78:79] op_sel_hi:[1,0]
	v_pk_fma_f32 v[10:11], v[62:63], v[76:77], v[10:11] op_sel:[0,1,0] op_sel_hi:[1,1,1]
	v_pk_fma_f32 v[12:13], v[64:65], v[76:77], v[12:13] op_sel:[0,1,0] op_sel_hi:[1,1,1]
	v_pk_mul_f32 v[36:37], v[10:11], v[10:11]
	v_pk_add_f32 v[34:35], v[10:11], v[12:13]
	v_pk_fma_f32 v[36:37], v[12:13], v[12:13], v[36:37]
	s_waitcnt lgkmcnt(2)
	v_pk_add_f32 v[14:15], v[14:15], v[54:55]
	v_pk_add_f32 v[16:17], v[16:17], v[56:57]
	v_pk_add_f32 v[14:15], v[14:15], v[78:79] op_sel_hi:[1,0]
	v_pk_add_f32 v[16:17], v[16:17], v[78:79] op_sel_hi:[1,0]
	v_pk_fma_f32 v[14:15], v[68:69], v[76:77], v[14:15] op_sel:[0,1,0] op_sel_hi:[1,1,1]
	v_pk_fma_f32 v[16:17], v[70:71], v[76:77], v[16:17] op_sel:[0,1,0] op_sel_hi:[1,1,1]
	v_pk_add_f32 v[34:35], v[34:35], v[14:15]
	v_pk_fma_f32 v[36:37], v[14:15], v[14:15], v[36:37]
	v_pk_add_f32 v[34:35], v[34:35], v[16:17]
	v_pk_fma_f32 v[36:37], v[16:17], v[16:17], v[36:37]
	s_waitcnt lgkmcnt(0)
	v_pk_add_f32 v[18:19], v[18:19], v[58:59]
	v_pk_add_f32 v[20:21], v[20:21], v[60:61]
	v_pk_add_f32 v[18:19], v[18:19], v[78:79] op_sel_hi:[1,0]
	v_pk_add_f32 v[20:21], v[20:21], v[78:79] op_sel_hi:[1,0]
	v_pk_fma_f32 v[18:19], v[72:73], v[76:77], v[18:19] op_sel:[0,1,0] op_sel_hi:[1,1,1]
	v_pk_fma_f32 v[20:21], v[74:75], v[76:77], v[20:21] op_sel:[0,1,0] op_sel_hi:[1,1,1]
	v_pk_add_f32 v[34:35], v[34:35], v[18:19]
	v_pk_fma_f32 v[36:37], v[18:19], v[18:19], v[36:37]
	v_pk_add_f32 v[34:35], v[34:35], v[20:21]
	v_pk_fma_f32 v[36:37], v[20:21], v[20:21], v[36:37]
	ds_read2st64_b32 v[50:51], v221 offset0:36 offset1:37
	ds_read2st64_b32 v[52:53], v221 offset0:38 offset1:39
	ds_read2st64_b32 v[62:63], v67 offset0:144 offset1:146
	ds_read2st64_b32 v[64:65], v67 offset0:148 offset1:150
	s_waitcnt lgkmcnt(0)
	v_pk_add_f32 v[22:23], v[22:23], v[50:51]
	v_pk_add_f32 v[24:25], v[24:25], v[52:53]
	v_pk_add_f32 v[22:23], v[22:23], v[78:79] op_sel_hi:[1,0]
	v_pk_add_f32 v[24:25], v[24:25], v[78:79] op_sel_hi:[1,0]
	v_pk_fma_f32 v[22:23], v[62:63], v[76:77], v[22:23] op_sel:[0,1,0] op_sel_hi:[1,1,1]
	v_pk_fma_f32 v[24:25], v[64:65], v[76:77], v[24:25] op_sel:[0,1,0] op_sel_hi:[1,1,1]
	v_pk_add_f32 v[34:35], v[34:35], v[22:23]
	v_pk_fma_f32 v[36:37], v[22:23], v[22:23], v[36:37]
	v_pk_add_f32 v[34:35], v[34:35], v[24:25]
	v_pk_fma_f32 v[36:37], v[24:25], v[24:25], v[36:37]
	s_mov_b64 s[40:41], exec
	s_and_b64 exec, exec, s[0:1]
	ds_read2st64_b32 v[50:51], v221 offset0:40 offset1:41
	ds_read2st64_b32 v[52:53], v221 offset0:42 offset1:43
	ds_read2st64_b32 v[62:63], v67 offset0:160 offset1:162
	ds_read2st64_b32 v[64:65], v67 offset0:164 offset1:166
	s_waitcnt lgkmcnt(0)
	v_pk_add_f32 v[26:27], v[26:27], v[50:51]
	v_pk_add_f32 v[28:29], v[28:29], v[52:53]
	v_pk_add_f32 v[26:27], v[26:27], v[78:79] op_sel_hi:[1,0]
	v_pk_add_f32 v[28:29], v[28:29], v[78:79] op_sel_hi:[1,0]
	v_pk_fma_f32 v[26:27], v[62:63], v[76:77], v[26:27] op_sel:[0,1,0] op_sel_hi:[1,1,1]
	v_pk_fma_f32 v[28:29], v[64:65], v[76:77], v[28:29] op_sel:[0,1,0] op_sel_hi:[1,1,1]
	v_pk_add_f32 v[34:35], v[34:35], v[26:27]
	v_pk_fma_f32 v[36:37], v[26:27], v[26:27], v[36:37]
	v_pk_add_f32 v[34:35], v[34:35], v[28:29]
	v_pk_fma_f32 v[36:37], v[28:29], v[28:29], v[36:37]
	s_mov_b64 exec, s[40:41]
	v_add_f32_e32 v34, v34, v35
	v_add_f32_e32 v36, v36, v37
	s_nop 1
	v_permlane32_swap_b32_e32 v34, v36
	v_add_f32_e32 v38, v34, v36
	ds_write_b32 v236, v38
